# NA attention: bid rotated so that an XCD owns 16 consecutive block rows (neighbouring rows share K/V)
# speedup vs baseline: 1.0025x; 1.0016x over previous
; __device__ __forceinline__ void phase_na_attention(const Params& P, float* sm, int bid, int nb) {
;     ...
;     const int lane = threadIdx.x & 63, wave = threadIdx.x >> 6, r = lane & 31, h = lane >> 5;
;     const float SC = 0.125f * 1.4426950408889634f, L2E = 1.4426950408889634f;
;     __syncthreads();
;     for (int e = threadIdx.x; e < 8 * 15 * 31; e += NTHR) sm[e] = P.in[12][e] * L2E;
;     __syncthreads();
;     for (int task = bid * 8 + wave; task < 260 * 16; task += nb * 8) {
;         const int qh = task & 1, head = (task >> 1) & 7, blk = task >> 4;
;         const bool lat = blk >= 4;
;         const int rr = blk - 4;
;         const int tok = blk * 64 + qh * 32 + r;
;         const int c = qh * 32 + r;
;         const int cs = min(max(c - 8, 0), 48), rs = min(max(rr - 4, 0), 248);
.LBB0_485:
	s_or_b64 exec, exec, s[0:1]
	s_mov_b32 s0, s44
	v_and_b32_e32 v180, 31, v0
	v_lshrrev_b32_e32 v2, 6, v0
	v_writelane_b32 v252, s0, 23
	v_readlane_b32 s96, v253, 10
	s_cmpk_lg_u32 s96, 0x100
	s_mov_b32 s96, s44
	s_cbranch_scc1 .Lna_xcd
	s_and_b32 s96, s44, 7
	s_lshl_b32 s96, s96, 5
	s_lshr_b32 s97, s44, 3
	s_or_b32 s96, s96, s97
.Lna_xcd:
	v_lshl_or_b32 v1, s96, 3, v2
	v_lshlrev_b32_e32 v181, 2, v180
	v_writelane_b32 v252, s1, 24
	s_movk_i32 s0, 0x1040
	s_waitcnt lgkmcnt(0)
	s_barrier
	v_cmp_gt_i32_e32 vcc, s0, v1
	s_mov_b64 s[0:1], exec
	v_writelane_b32 v252, s0, 25
	s_nop 1
	v_writelane_b32 v252, s1, 26
	s_and_b64 s[0:1], s[0:1], vcc
	s_mov_b64 exec, s[0:1]
	s_cbranch_execz .LBB0_638
	v_readlane_b32 s0, v252, 19
	v_readlane_b32 s2, v252, 21
	v_readlane_b32 s3, v252, 22
	s_add_u32 s42, s2, 0x3f622400
	s_addc_u32 s43, s3, 0
	s_add_u32 s44, s2, 0x3c562400
	s_addc_u32 s45, s3, 0
	v_readlane_b32 s1, v252, 20
	s_add_u32 s0, s2, 0xf278000
	s_addc_u32 s1, s3, 0
	v_writelane_b32 v252, s0, 27
	v_mbcnt_lo_u32_b32 v5, -1, 0
	v_mbcnt_hi_u32_b32 v5, -1, v5
	v_writelane_b32 v252, s1, 28
	s_add_u32 s0, s2, 0x7078000
	s_addc_u32 s1, s3, 0
	v_bfe_u32 v3, v0, 5, 1
	v_and_b32_e32 v7, 64, v5
	v_readlane_b32 s2, v253, 10
	v_lshlrev_b32_e32 v4, 3, v3
	v_xor_b32_e32 v6, 32, v5
	v_add_u32_e32 v7, 64, v7
	v_lshlrev_b32_e32 v186, 2, v3
	s_mov_b32 s4, s2
	s_lshl_b32 s2, s2, 3
	v_lshlrev_b32_e32 v3, 4, v3
	v_mov_b32_e32 v185, 0
	v_cmp_lt_i32_e32 vcc, v6, v7
	v_readlane_b32 s3, v253, 11
	v_writelane_b32 v252, s2, 29
	v_sub_u32_e32 v3, v3, v181
	v_cndmask_b32_e32 v5, v5, v6, vcc
	v_lshlrev_b32_e32 v188, 4, v202
	v_mov_b32_e32 v189, v185
	v_add_u32_e32 v3, 0, v3
	v_lshlrev_b32_e32 v2, 5, v2
	v_readlane_b32 s2, v252, 23
	v_lshlrev_b32_e32 v179, 2, v5
	v_or_b32_e32 v190, 0x400, v188
	v_mov_b32_e32 v191, v185
	v_or_b32_e32 v183, 1, v186
	v_or_b32_e32 v187, 2, v186
	v_or_b32_e32 v203, 3, v186
	v_or_b32_e32 v207, 8, v186
	v_or_b32_e32 v210, 9, v186
	v_or_b32_e32 v211, 10, v186
	v_or_b32_e32 v212, 11, v186
	v_or_b32_e32 v213, 16, v186
	v_or_b32_e32 v214, 17, v186
	v_or_b32_e32 v215, 18, v186
	v_or_b32_e32 v216, 19, v186
	v_or_b32_e32 v217, 24, v186
	v_or_b32_e32 v218, 25, v186
	v_or_b32_e32 v219, 26, v186
	v_or_b32_e32 v220, 27, v186
	v_or_b32_e32 v221, 32, v186
	v_or_b32_e32 v222, 33, v186
	v_or_b32_e32 v223, 34, v186
	v_or_b32_e32 v224, 35, v186
	v_or_b32_e32 v225, 40, v186
	v_or_b32_e32 v226, 41, v186
	v_or_b32_e32 v227, 42, v186
	v_or_b32_e32 v228, 43, v186
	v_or_b32_e32 v229, 48, v186
	v_or_b32_e32 v230, 49, v186
	v_or_b32_e32 v231, 50, v186
	v_or_b32_e32 v232, 51, v186
	v_or_b32_e32 v233, 56, v186
	v_or_b32_e32 v234, 57, v186
	v_or_b32_e32 v235, 58, v186
	v_or_b32_e32 v236, 59, v186
	v_lshl_add_u64 v[192:193], s[42:43], 0, v[188:189]
	v_or_b32_e32 v194, 0x100, v202
	v_mov_b32_e32 v195, v185
	v_add_u32_e32 v237, 0x5a0, v3
	v_lshl_or_b32 v238, s2, 8, v2
	s_lshl_b32 s61, s4, 8
	s_mov_b64 s[78:79], 0
	v_lshlrev_b32_e32 v196, 1, v4
	s_mov_b64 s[56:57], 0x1000
	s_mov_b64 s[58:59], 0x1800
	s_mov_b32 s60, 0x3e38aa3b
	v_lshlrev_b32_e32 v198, 1, v186
	v_mov_b64_e32 v[200:201], s[0:1]
	v_mov_b32_e32 v197, v185
	v_mov_b32_e32 v239, 0xfffffe00
	v_mov_b32_e32 v240, 0xc0
	v_mov_b32_e32 v241, 0x100
	v_readlane_b32 s3, v252, 24
	s_branch .LBB0_489
